# baseline (speedup 1.0000x reference)
.LBB2_12:
	s_cmp_lt_i32 s64, s79
	s_cbranch_scc1 .Lattn_do_dma2

.Lattn_do_dma:
	s_xor_b32 s48, s37, 0x4000
	s_add_i32 s48, s78, s48
	s_mov_b32 m0, s48
	s_nop 0
	global_load_lds_dwordx4 v64, s[68:69]
	s_add_i32 m0, s48, 0x400
	s_nop 0
	global_load_lds_dwordx4 v65, s[68:69]
	s_branch .Lattn_no_dma
.Lattn_do_dma2:
	s_xor_b32 s48, s37, 0x4000
	s_add_i32 s48, s78, s48
	s_add_i32 m0, s48, 0x2000
	s_nop 0
	global_load_lds_dwordx4 v64, s[74:75]
	s_add_i32 m0, s48, 0x2400
	s_nop 0
	global_load_lds_dwordx4 v65, s[74:75]
	s_branch .Lattn_dma2_done
